# static s_setprio 1 for waves 4-7 also during the chunked-recurrence pass A + attention
# speedup vs baseline: 1.0160x; 1.0160x over previous
; DI void phase_chunkA(const Args& a, LAS unsigned char* lds, int wave, int lane, int tid, int bid, int G) {
;     ...
;     if (bid < NCHUNK) { const int c0_ = bid % NCK, bh0_ = bid / NCK; CK_LOADIN(c0_, bh0_ & 15, bh0_ >> 4); }
.LBB0_1006:
	s_or_b64 exec, exec, s[2:3]
	v_readfirstlane_b32 s2, v0
	s_cmpk_lt_u32 s2, 0x100
	s_cbranch_scc1 .Lprio_ca
	s_setprio 1
.Lprio_ca:
	s_add_u32 s2, s96, 0xf460000
	s_addc_u32 s3, s97, 0
	v_mov_b32_e32 v90, v91
	v_writelane_b32 v255, s2, 36
	v_mov_b32_e32 v92, v91
	v_mov_b32_e32 v93, v91
	v_mov_b64_e32 v[34:35], v[90:91]
	v_writelane_b32 v255, s3, 37
	v_mov_b64_e32 v[36:37], v[92:93]
	s_and_saveexec_b64 s[2:3], vcc
	s_cbranch_execz .LBB0_1008
	v_readlane_b32 s4, v255, 36
	v_readlane_b32 s5, v255, 37
	s_nop 1
	v_lshl_add_u64 v[4:5], v[2:3], 1, s[4:5]
	global_load_dwordx4 v[34:37], v[4:5], off

; __device__ __forceinline__ unsigned xb_add(unsigned* p, unsigned v) { return __hip_atomic_fetch_add(p, v, __ATOMIC_RELAXED, __HIP_MEMORY_SCOPE_AGENT); }
; __device__ __forceinline__ void xcd_barrier(const XcdBarrier& b) {
;     asm volatile("s_waitcnt vmcnt(0)" ::: "memory");
;     __syncthreads();
;     if (threadIdx.x == 0) {
;         unsigned* bar = b.bar;
;         __builtin_amdgcn_s_waitcnt(0);
;         unsigned nloc = b.st[0], nx = b.st[1];
;         if (nloc == 0u) { xcd_barrier_complete(bar, b.x, nloc, nx); b.st[0] = nloc; b.st[1] = nx; }
;         const unsigned old = xb_add(&bar[XB_XSUB(b.x)], 1u);
.LBB0_1095:
	s_setprio 0
	s_waitcnt vmcnt(0)
	s_waitcnt lgkmcnt(0)
	s_barrier
	s_mov_b64 s[8:9], exec
	v_readlane_b32 s0, v255, 21
	v_readlane_b32 s1, v255, 22
	s_and_b64 s[0:1], s[8:9], s[0:1]
	s_mov_b64 exec, s[0:1]
	s_cbranch_execz .LBB0_1143
	v_readlane_b32 s0, v254, 0
	s_waitcnt vmcnt(0) expcnt(0) lgkmcnt(0)
	s_nop 0
	v_mov_b32_e32 v2, s0
	ds_read_b32 v4, v2
	ds_read_b32 v2, v2 offset:4
	s_waitcnt lgkmcnt(1)
	v_cmp_ne_u32_e32 vcc, 0, v4
	s_cbranch_vccnz .LBB0_1111
	s_load_dwordx2 s[0:1], s[78:79], 0x4
	s_waitcnt lgkmcnt(0)
	s_mul_i32 s0, s0, s64
	s_mul_i32 s0, s0, s1
	s_mov_b32 s1, 1
	s_branch .LBB0_1099
